# static s_setprio 1 for waves 4-7 in attention units (on top of mfix routepfx peel0 cvdelta sink)
# baseline (speedup 1.0000x reference)
.LBB0_1063:
	s_mul_hi_i32 s26, s13, 0x55555556
	s_lshr_b32 s27, s26, 31
	s_add_i32 s28, s26, s27
	s_mul_i32 s27, s58, 0x1100000
	s_mul_hi_i32 s26, s58, 0x1100000
	s_add_u32 s29, s66, s27
	s_addc_u32 s34, s67, s26
	s_and_b64 s[26:27], exec, s[24:25]
	s_movk_i32 s26, 0xb00
	s_cselect_b32 s26, 0x600, s26
	s_add_u32 s29, s29, s26
	s_addc_u32 s34, s34, 0
	s_lshl_b32 s26, s13, 6
	s_ashr_i32 s27, s26, 31
	s_lshl_b64 s[26:27], s[26:27], 1
	s_add_u32 s40, s29, s26
	s_addc_u32 s41, s34, s27
	s_lshl_b32 s12, s12, 4
	s_lshl_b32 s13, s58, 1
	s_add_i32 s12, s12, s28
	s_add_i32 s12, s12, s13
	s_mul_hi_i32 s13, s12, 0x88000
	s_mul_i32 s12, s12, 0x88000
	s_waitcnt lgkmcnt(0)
	s_add_u32 s8, s8, s12
	s_addc_u32 s9, s9, s13
	s_add_u32 s10, s10, s12
	s_waitcnt vmcnt(11)
	v_mbcnt_lo_u32_b32 v36, -1, 0
	v_mbcnt_hi_u32_b32 v36, -1, v36
	s_getreg_b32 s12, hwreg(HW_REG_HW_ID, 0, 6)
	s_addc_u32 s11, s11, s13
	s_lshl_b32 s12, s12, 2
	s_and_b32 s12, s12, 0xfc
	s_or_b32 s12, s12, 0x27100
	v_mov_b32_e32 v0, s12
	ds_read_b32 v0, v0
	s_and_b64 vcc, s[6:7], s[24:25]
	v_and_b32_e32 v211, 63, v36
	v_and_b32_e32 v231, 31, v36
	v_bfe_u32 v232, v36, 5, 1
	s_waitcnt lgkmcnt(0)
	v_readfirstlane_b32 s12, v0
	v_lshlrev_b32_e32 v0, 7, v211
	v_lshl_add_u64 v[2:3], s[8:9], 0, v[0:1]
	v_lshl_or_b32 v4, s12, 6, v36
	v_bfe_u32 v0, v36, 2, 4
	v_readfirstlane_b32 s13, v4
	s_ashr_i32 s89, s13, 6
	s_cmp_lt_u32 s89, 4
	s_cbranch_scc1 .Lat_prio_skip
	s_setprio 1
.Lat_prio_skip:
	s_lshl_b32 s37, s89, 5
	s_add_i32 s28, s37, s36
	s_ashr_i32 s29, s28, 31
	s_lshl_b64 s[34:35], s[28:29], 12
	s_add_u32 s34, s40, s34
	s_addc_u32 s35, s41, s35
	s_lshl_b32 s8, s89, 3
	s_ashr_i32 s9, s8, 31
	v_lshl_add_u64 v[2:3], s[8:9], 1, v[2:3]
	s_mov_b64 s[8:9], 0x5a800000
	v_lshl_add_u64 v[206:207], v[2:3], 0, s[8:9]
	s_lshl_b32 s8, s89, 4
	v_and_or_b32 v0, s8, 48, v0
	s_ashr_i32 s8, s13, 3
	v_lshlrev_b32_e32 v0, 7, v0
	s_andn2_b32 s8, s8, 31
	v_lshlrev_b32_e32 v230, 3, v4
	v_lshl_add_u64 v[2:3], s[10:11], 0, v[0:1]
	s_ashr_i32 s9, s8, 31
	v_and_b32_e32 v234, 24, v230
	v_lshl_add_u64 v[2:3], s[8:9], 1, v[2:3]
	v_lshlrev_b32_e32 v0, 1, v234
	s_lshl_b32 s12, s89, 10
	v_lshl_add_u64 v[2:3], v[2:3], 0, v[0:1]
	s_mov_b64 s[8:9], 0x5cc00000
	s_cmp_lg_u32 0, -1
	v_lshl_add_u64 v[208:209], v[2:3], 0, s[8:9]
	s_cselect_b32 s8, 0, 0
	s_lshl_b32 s70, s69, 7
	s_add_i32 s45, s12, s8
	v_lshl_add_u64 v[34:35], v[206:207], 0, s[70:71]
	s_mov_b32 s8, m0
	s_mov_b32 m0, s45
	s_nop 0
	global_load_lds_dwordx4 v[34:35], off
	s_mov_b32 m0, s8
	s_add_i32 s44, s45, 0x6000
	v_lshl_add_u64 v[2:3], v[208:209], 0, s[70:71]
	s_mov_b32 s8, m0
	s_mov_b32 m0, s44
	s_nop 0
	global_load_lds_dwordx4 v[2:3], off
	s_mov_b32 m0, s8
	s_bitset1_b32 s70, 13
	v_lshlrev_b32_e32 v0, 12, v231
	v_lshl_add_u64 v[2:3], v[206:207], 0, s[70:71]
	s_add_i32 s8, s45, 0x2000
	s_mov_b32 s9, m0
	s_mov_b32 m0, s8
	s_nop 0
	global_load_lds_dwordx4 v[2:3], off
	s_mov_b32 m0, s9
	v_lshl_or_b32 v0, v232, 4, v0
	global_load_dwordx4 v[152:155], v0, s[34:35]
	global_load_dwordx4 v[144:147], v0, s[34:35] offset:32
	global_load_dwordx4 v[132:135], v0, s[34:35] offset:64
	global_load_dwordx4 v[128:131], v0, s[34:35] offset:96
	v_mov_b32_e32 v2, v1
	v_mov_b32_e32 v3, v1
	v_mov_b32_e32 v4, v1
	v_mov_b32_e32 v5, v1
	v_mov_b32_e32 v6, v1
	v_mov_b32_e32 v7, v1
	v_mov_b32_e32 v8, v1
	v_mov_b32_e32 v9, v1
	v_mov_b32_e32 v10, v1
	v_mov_b32_e32 v11, v1
	v_mov_b32_e32 v12, v1
	v_mov_b32_e32 v13, v1
	v_mov_b32_e32 v14, v1
	v_mov_b32_e32 v15, v1
	v_lshlrev_b32_e32 v0, 10, v232
	v_lshlrev_b32_e32 v16, 4, v231
	v_add3_u32 v240, 0, v0, v16
	v_mov_b32_e32 v0, v1
	v_mov_b64_e32 v[16:17], v[14:15]
	v_mov_b64_e32 v[14:15], v[12:13]
	v_mov_b64_e32 v[12:13], v[10:11]
	v_mov_b64_e32 v[10:11], v[8:9]
	v_mov_b64_e32 v[8:9], v[6:7]
	v_mov_b64_e32 v[6:7], v[4:5]
	v_mov_b64_e32 v[4:5], v[2:3]
	v_mov_b64_e32 v[2:3], v[0:1]
	s_mov_b64 s[8:9], 0x4000
	v_lshl_add_u64 v[18:19], v[34:35], 0, s[8:9]
	s_add_i32 s8, s45, 0x4000
	s_mov_b32 s9, m0
	s_mov_b32 m0, s8
	s_nop 0
	global_load_lds_dwordx4 v[18:19], off
	s_mov_b32 m0, s9
	s_waitcnt vmcnt(3) lgkmcnt(0)
	s_barrier
	s_waitcnt vmcnt(14)
	ds_read_b128 v[38:41], v240
	v_cndmask_b32_e32 v0, 0, v210, vcc
	v_cmp_nlt_f32_e64 s[8:9], 0, v0
	s_and_b64 vcc, exec, s[8:9]
	s_waitcnt vmcnt(3) lgkmcnt(0)
	v_mfma_f32_32x32x16_bf16 v[18:33], v[38:41], v[152:155], v[2:17]
	ds_read_b128 v[38:41], v240 offset:512
	s_waitcnt lgkmcnt(0)
	v_mfma_f32_32x32x16_bf16 v[2:17], v[38:41], v[152:155], v[2:17]
	ds_read_b128 v[38:41], v240 offset:2048
	s_waitcnt vmcnt(2) lgkmcnt(0)
	v_mfma_f32_32x32x16_bf16 v[18:33], v[38:41], v[144:147], v[18:33]
	ds_read_b128 v[38:41], v240 offset:2560
	s_waitcnt lgkmcnt(0)
	v_mfma_f32_32x32x16_bf16 v[2:17], v[38:41], v[144:147], v[2:17]
	ds_read_b128 v[38:41], v240 offset:4096
	s_waitcnt vmcnt(1) lgkmcnt(0)
	v_mfma_f32_32x32x16_bf16 v[18:33], v[38:41], v[132:135], v[18:33]
	ds_read_b128 v[38:41], v240 offset:4608
	s_waitcnt lgkmcnt(0)
	v_mfma_f32_32x32x16_bf16 v[2:17], v[38:41], v[132:135], v[2:17]
	ds_read_b128 v[38:41], v240 offset:6144
	s_waitcnt vmcnt(0) lgkmcnt(0)
	v_mfma_f32_32x32x16_bf16 v[18:33], v[38:41], v[128:131], v[18:33]
	ds_read_b128 v[38:41], v240 offset:6656
	s_waitcnt lgkmcnt(0)
	v_mfma_f32_32x32x16_bf16 v[2:17], v[38:41], v[128:131], v[2:17]
	s_nop 15
	s_nop 7
	s_cbranch_vccz .LBB0_1065
	v_max3_f32 v37, v18, v19, v2
	v_max3_f32 v38, v20, v21, v3
	s_nop 0
	v_max3_f32 v37, v37, v4, v5
	v_max3_f32 v38, v38, v24, v25
	s_nop 0
	v_max3_f32 v37, v37, v22, v23
	v_max3_f32 v38, v38, v8, v9
	s_nop 0
	v_max3_f32 v37, v37, v6, v7
	v_max3_f32 v38, v38, v28, v29
	s_nop 0
	v_max3_f32 v37, v37, v26, v27
	v_max3_f32 v38, v38, v12, v13
	s_nop 0
	v_max3_f32 v37, v37, v10, v11
	v_max3_f32 v38, v38, v32, v33
	s_nop 0
	v_max3_f32 v37, v37, v30, v31
	v_max3_f32 v38, v38, v16, v17
	s_nop 0
	v_max3_f32 v37, v37, v14, v15
	s_nop 0
	v_max_f32_e32 v37, v37, v38
	s_nop 0
	v_mov_b32_e32 v38, v37
	s_nop 1
	v_permlane32_swap_b32_e32 v37, v38
	v_max_f32_e32 v37, v37, v38
	s_cbranch_execz .LBB0_1066
	s_branch .LBB0_1067

.LBB0_1155:
	s_setprio 0
	s_movk_i32 s6, 0x48
	s_barrier
	s_ashr_i32 s7, s6, 31
	s_lshl_b64 s[6:7], s[6:7], 2
	s_add_u32 s6, s0, s6
	s_addc_u32 s7, s1, s7
	s_load_dwordx2 s[8:9], s[6:7], 0x0
	s_waitcnt lgkmcnt(0)
	s_cmp_le_i32 s8, s42
	s_cselect_b64 s[6:7], -1, 0
	s_cmp_lt_i32 s42, s9
	s_cselect_b64 s[8:9], -1, 0
	s_and_b64 s[6:7], s[6:7], s[8:9]
	s_andn2_b64 vcc, exec, s[6:7]
	s_cbranch_vccnz .LBB0_1210
	s_mul_i32 s6, s73, 10
	s_add_i32 s10, s6, 5
	s_movk_i32 s6, 0x48
	s_ashr_i32 s7, s6, 31
	s_lshl_b64 s[6:7], s[6:7], 2
	s_add_u32 s6, s0, s6
	s_addc_u32 s7, s1, s7
	s_load_dwordx2 s[8:9], s[6:7], 0x0
	s_waitcnt lgkmcnt(0)
	s_cmp_le_i32 s8, s10
	s_cselect_b64 s[6:7], -1, 0
	s_cmp_lt_i32 s10, s9
	s_cselect_b64 s[8:9], -1, 0
	s_and_b64 s[6:7], s[6:7], s[8:9]
	s_andn2_b64 vcc, exec, s[6:7]
	s_cbranch_vccnz .LBB0_1210
	s_mov_b32 s8, 35
	s_getreg_b32 s10, hwreg(HW_REG_XCC_ID, 0, 4)
	s_waitcnt vmcnt(0)
	s_barrier
	s_mov_b64 s[6:7], exec
	v_readlane_b32 s12, v255, 31
	v_readlane_b32 s13, v255, 32
	s_and_b64 s[12:13], s[6:7], s[12:13]
	s_mov_b64 exec, s[12:13]
	s_cbranch_execz .LBB0_1209
	s_ashr_i32 s9, s8, 31
	s_lshl_b64 s[8:9], s[8:9], 3
	s_add_u32 s8, s0, s8
	v_readlane_b32 s11, v254, 56
	s_addc_u32 s9, s1, s9
	s_load_dwordx2 s[8:9], s[8:9], 0x0
	v_mov_b32_e32 v0, s11
	s_waitcnt vmcnt(0) expcnt(0) lgkmcnt(0)
	ds_read_b32 v3, v0
	v_readlane_b32 s11, v254, 57
	s_and_b32 s44, s10, 15
	s_waitcnt lgkmcnt(0)
	v_cmp_ne_u32_e32 vcc, 0, v3
	v_mov_b32_e32 v0, s11
	ds_read_b32 v2, v0
	s_cbranch_vccnz .LBB0_1173
	v_readlane_b32 s10, v254, 0
	v_readlane_b32 s11, v254, 1
	s_load_dwordx2 s[14:15], s[10:11], 0x4
	s_add_u32 s10, s8, 0x4200
	s_addc_u32 s11, s9, 0
	s_add_u32 s12, s8, 0x4400
	s_addc_u32 s13, s9, 0
	s_waitcnt lgkmcnt(0)
	s_mul_i32 s45, s14, s3
	s_add_u32 s14, s8, 0x4500
	s_mul_i32 s45, s45, s15
	s_addc_u32 s15, s9, 0
	s_add_u32 s16, s8, 0x4600
	s_addc_u32 s17, s9, 0
	s_add_u32 s18, s8, 0x4700
	s_addc_u32 s19, s9, 0
	s_add_u32 s20, s8, 0x4800
	s_addc_u32 s21, s9, 0
	s_add_u32 s22, s8, 0x4900
	s_addc_u32 s23, s9, 0
	s_add_u32 s24, s8, 0x4a00
	s_addc_u32 s25, s9, 0
	s_add_u32 s26, s8, 0x4b00
	s_addc_u32 s27, s9, 0
	s_add_u32 s28, s8, 0x4c00
	s_addc_u32 s29, s9, 0
	s_add_u32 s30, s8, 0x4d00
	s_addc_u32 s31, s9, 0
	s_add_u32 s34, s8, 0x4e00
	s_addc_u32 s35, s9, 0
	s_add_u32 s36, s8, 0x4f00
	s_addc_u32 s37, s9, 0
	s_add_u32 s92, s8, 0x5000
	s_addc_u32 s93, s9, 0
	s_add_u32 s94, s8, 0x5100
	s_addc_u32 s95, s9, 0
	s_add_u32 s96, s8, 0x5200
	s_addc_u32 s97, s9, 0
	s_add_u32 s42, s8, 0x5300
	s_addc_u32 s43, s9, 0
	s_mov_b32 s46, 1
	s_branch .LBB0_1161
